# baseline (speedup 1.0000x reference)
_ZN12_GLOBAL__N_113search_kernelEPKfS1_PhPf:
	s_load_dwordx2 s[8:9], s[0:1], 0x0
	s_load_dwordx2 s[4:5], s[0:1], 0x10
	s_movk_i32 s3, 0x90
	v_readfirstlane_b32 s10, v0
	v_cmp_gt_u32_e32 vcc, s3, v0
	s_and_saveexec_b64 s[6:7], vcc
	v_mov_b32_e32 v2, -1
	v_lshlrev_b32_e32 v1, 3, v0
	v_mov_b32_e32 v3, v2
	ds_write_b64 v1, v[2:3] offset:16384
	s_or_b64 exec, exec, s[6:7]
	s_waitcnt lgkmcnt(0)
	s_add_u32 s6, s4, 0x240000
	s_addc_u32 s7, s5, 0
	s_lshl_b32 s11, s2, 1
	s_and_b32 s14, s11, 14
	s_ashr_i32 s11, s2, 7
	s_lshr_b32 s15, s10, 6
	s_add_i32 s14, s14, s11
	s_bfe_u32 s2, s2, 0x40003
	s_mul_i32 s11, s15, 24
	v_mul_u32_u24_e32 v2, 0x71d, v0
	v_mul_u32_u24_e32 v4, 0x195, v0
	s_min_u32 s18, s11, 0xa5
	s_mul_i32 s11, s14, 3
	s_mul_i32 s12, s2, 9
	s_mov_b32 s13, 0
	v_lshrrev_b32_e32 v3, 16, v2
	s_movk_i32 s19, 0xffdc
	v_lshrrev_b32_e32 v5, 17, v4
	v_mad_i32_i24 v2, v3, s19, v0
	v_mad_i32_i24 v4, v5, -9, v3
	v_add_u32_e32 v3, s11, v5
	v_mov_b64_e32 v[6:7], s[12:13]
	v_mad_i64_i32 v[8:9], s[16:17], v3, s3, v[6:7]
	v_ashrrev_i32_e32 v5, 31, v4
	v_lshl_add_u64 v[4:5], v[8:9], 0, v[4:5]
	s_movk_i32 s13, 0x240
	v_mov_b64_e32 v[8:9], s[8:9]
	v_mad_u64_u32 v[10:11], s[8:9], v4, s13, v[8:9]
	v_min_u32_e32 v4, 0x1cb, v0
	v_or_b32_e32 v4, 0x200, v4
	v_mad_i32_i24 v11, v5, s13, v11
	v_mul_u32_u24_e32 v5, 0x71d, v4
	v_ashrrev_i32_e32 v3, 31, v2
	v_lshrrev_b32_e32 v5, 16, v5
	v_lshl_add_u64 v[2:3], v[2:3], 4, v[10:11]
	v_mad_i32_i24 v10, v5, s19, v4
	v_mul_u32_u24_e32 v4, 0x653, v4
	v_lshrrev_b32_e32 v11, 19, v4
	v_mad_i32_i24 v4, v11, -9, v5
	v_add_u32_e32 v5, s11, v11
	v_mad_i64_i32 v[6:7], s[8:9], v5, s3, v[6:7]
	v_ashrrev_i32_e32 v5, 31, v4
	v_lshl_add_u64 v[4:5], v[6:7], 0, v[4:5]
	v_mad_u64_u32 v[12:13], s[8:9], v4, s13, v[8:9]
	s_mul_i32 s8, s14, 0x90
	s_barrier
	s_load_dwordx2 s[42:43], s[0:1], 0x8
	v_mov_b32_e32 v16, 0
	v_mov_b32_e32 v17, 0
	ds_write_b64 v16, v[16:17] offset:18112
	global_load_dwordx4 v[6:9], v[2:3], off
	v_mad_i32_i24 v13, v5, s13, v13
	v_ashrrev_i32_e32 v11, 31, v10
	v_lshl_add_u64 v[10:11], v[10:11], 4, v[12:13]
	global_load_dwordx4 v[10:13], v[10:11], off
	v_and_b32_e32 v1, 63, v0
	s_add_i32 s20, s8, s12
	s_lshl_b32 s20, s20, 10
	v_lshl_add_u32 v164, v1, 4, s20
	s_mul_i32 s9, s14, 0xbd
	s_add_i32 s21, s9, s18
	s_lshl_b32 s21, s21, 10
	v_lshl_add_u32 v165, v1, 4, s21
	s_add_u32 s22, s4, 0x1000
	s_addc_u32 s23, s5, 0
	s_add_u32 s24, s4, 0x2000
	s_addc_u32 s25, s5, 0
	s_mov_b32 s26, s6
	s_mov_b32 s27, s7
	s_add_u32 s28, s6, 0x1000
	s_addc_u32 s29, s7, 0
	s_add_u32 s30, s6, 0x2000
	s_addc_u32 s31, s7, 0
	s_add_u32 s32, s6, 0x3000
	s_addc_u32 s33, s7, 0
	s_add_u32 s34, s6, 0x4000
	s_addc_u32 s35, s7, 0
	s_add_u32 s36, s6, 0x5000
	s_addc_u32 s37, s7, 0
	v_bfe_u32 v166, v0, 4, 2
	v_and_b32_e32 v167, 15, v0
	v_lshlrev_b32_e32 v167, 3, v167
	s_mul_i32 s40, s15, 6
	s_mov_b32 s41, 0x7f000000
	global_load_dwordx4 v[112:115], v164, s[4:5]
	global_load_dwordx4 v[16:19], v165, s[26:27] nt
	global_load_dwordx4 v[20:23], v165, s[26:27] offset:1024 nt
	global_load_dwordx4 v[24:27], v165, s[26:27] offset:2048 nt
	global_load_dwordx4 v[28:31], v165, s[26:27] offset:3072 nt
	global_load_dwordx4 v[32:35], v165, s[28:29] nt
	global_load_dwordx4 v[36:39], v165, s[28:29] offset:1024 nt
	global_load_dwordx4 v[40:43], v165, s[28:29] offset:2048 nt
	global_load_dwordx4 v[44:47], v165, s[28:29] offset:3072 nt
	global_load_dwordx4 v[48:51], v165, s[30:31] nt
	global_load_dwordx4 v[52:55], v165, s[30:31] offset:1024 nt
	global_load_dwordx4 v[56:59], v165, s[30:31] offset:2048 nt
	global_load_dwordx4 v[60:63], v165, s[30:31] offset:3072 nt
	global_load_dwordx4 v[64:67], v165, s[32:33] nt
	global_load_dwordx4 v[68:71], v165, s[32:33] offset:1024 nt
	global_load_dwordx4 v[72:75], v165, s[32:33] offset:2048 nt
	global_load_dwordx4 v[76:79], v165, s[32:33] offset:3072 nt
	global_load_dwordx4 v[80:83], v165, s[34:35] nt
	global_load_dwordx4 v[84:87], v165, s[34:35] offset:1024 nt
	global_load_dwordx4 v[88:91], v165, s[34:35] offset:2048 nt
	global_load_dwordx4 v[92:95], v165, s[34:35] offset:3072 nt
	global_load_dwordx4 v[96:99], v165, s[36:37] nt
	global_load_dwordx4 v[100:103], v165, s[36:37] offset:1024 nt
	global_load_dwordx4 v[104:107], v165, s[36:37] offset:2048 nt
	global_load_dwordx4 v[108:111], v165, s[36:37] offset:3072 nt
	global_load_dwordx4 v[116:119], v164, s[4:5] offset:1024
	v_lshlrev_b32_e32 v14, 4, v0
	s_lshr_b32 s50, s15, 1
	s_and_b32 s51, s15, 1
	s_lshl_b32 s51, s51, 3
	s_mov_b32 s48, 0x1010101
	s_mov_b32 s49, 0x1010101
	s_movk_i32 s58, 0x900
	s_movk_i32 s59, 0xb40
	v_and_b32_e32 v168, 7, v0
	v_lshrrev_b32_e32 v177, 3, v1
	v_or_b32_e32 v177, s51, v177
	v_lshlrev_b32_e32 v169, 3, v177
	v_and_b32_e32 v179, 3, v0
	v_lshlrev_b32_e32 v179, 8, v179
	v_lshl_add_u32 v170, v177, 4, v179
	v_add_u32_e32 v170, s20, v170
	v_lshrrev_b32_e32 v179, 2, v168
	v_and_b32_e32 v180, 3, v0
	v_lshl_or_b32 v171, v179, 4, v180
	v_mul_u32_u24_e32 v179, 11, v168
	v_lshrrev_b32_e32 v179, 5, v179
	v_mul_u32_u24_e32 v180, 3, v179
	v_sub_u32_e32 v180, v168, v180
	v_mul_u32_u24_e32 v181, 0x90, v179
	v_add_u32_e32 v181, v181, v180
	v_mul_u32_u24_e32 v172, 0x240, v181
	v_mul_u32_u24_e32 v181, 0x48, v179
	v_add_u32_e32 v181, v181, v180
	v_mul_u32_u24_e32 v173, 0x120, v181
	v_mul_u32_u24_e32 v181, 0x24, v179
	v_add_u32_e32 v181, v181, v180
	v_mul_u32_u24_e32 v174, 0x90, v181
	v_mul_u32_u24_e32 v181, 9, v179
	v_add_u32_e32 v181, v181, v180
	v_mul_u32_u24_e32 v175, 0x240, v181
	v_add_u32_e32 v176, 8, v168
	s_waitcnt lgkmcnt(0)
	s_mul_i32 s60, s14, 0x3cc00
	s_add_u32 s42, s42, s60
	s_addc_u32 s43, s43, 0
	s_mul_i32 s60, s14, 0xf300
	s_add_u32 s44, s4, s60
	s_addc_u32 s45, s5, 0
	s_add_u32 s44, s44, 0x534000
	s_addc_u32 s45, s45, 0
	s_mul_i32 s60, s14, 0x3cc0
	s_add_u32 s46, s4, s60
	s_addc_u32 s47, s5, 0
	s_add_u32 s46, s46, 0x627000
	s_addc_u32 s47, s47, 0
	v_mov_b32_e32 v152, s42
	v_mov_b32_e32 v153, s43
	v_mov_b32_e32 v154, s44
	v_mov_b32_e32 v155, s45
	v_mov_b32_e32 v159, s46
	v_mov_b32_e32 v161, s47
	s_load_dwordx2 s[2:3], s[0:1], 0x18
	s_cmp_lt_u32 s15, 4
	s_cbranch_scc0 .Lprio_done
	s_setprio 1
